# N2: all 24 modulation-vector loads issued together instead of 12 serialized round trips (on top of nt conversion hints)
# speedup vs baseline: 1.0063x; 1.0016x over previous
; #define GAS __attribute__((address_space(1)))
; __device__ __forceinline__ void n2_phase(const Frame& F0, int L, int nrows) {
;     ...
;     for (int g = 0; g < NG;) {
;       int gend = NG;
;       { const int row0_ = rb + 16 * g, bm = row0_ < NLAT ? (row0_ >> 11) : 16; const float* mrow = modL + bm * 6144;
;         if (row0_ < NLAT) { const int ge = ((((row0_ >> 11) + 1) << 11) - rb) >> 4; gend = ge < NG ? ge : NG; }
; #pragma unroll
;         for (int s_ = 0; s_ < 4; ++s_)
; #pragma unroll
;             for (int q = 0; q < 2; ++q) { const int c = c0 + 32 * s_ + 4 * q; gs[s_][q] = *(const GAS f32x4*)(gn + c) * (*(const GAS f32x4*)(mrow + 4 * 1024 + c) + 1.0f); sh[s_][q] = *(const GAS f32x4*)(mrow + 3 * 1024 + c); } }
;       for (; g < gend; ++g) {
;         const int row0 = rb + 16 * g, row = row0 + r, par = g & 1;
;         f32x4 v[4][2];
; #pragma unroll
;         for (int s_ = 0; s_ < 4; ++s_) { v[s_][0] = (f32x4){bf_lo(nraw[s_].x), bf_hi(nraw[s_].x), bf_lo(nraw[s_].y), bf_hi(nraw[s_].y)}; v[s_][1] = (f32x4){bf_lo(nraw[s_].z), bf_hi(nraw[s_].z), bf_lo(nraw[s_].w), bf_hi(nraw[s_].w)}; }
.LBB0_1204:
	s_lshl_b32 s8, s7, 4
	s_add_i32 s2, s8, s4
	s_and_b32 s0, s2, 0xfffff800
	s_sub_i32 s0, s0, s4
	s_addk_i32 s0, 0x800
	s_ashr_i32 s0, s0, 4
	s_min_i32 s3, s0, s5
	s_cmp_lt_i32 s2, 0x8000
	s_cselect_b64 s[0:1], -1, 0
	s_and_b64 s[10:11], s[0:1], exec
	s_cselect_b32 s6, s3, s5
	s_cmp_ge_i32 s7, s6
	s_cbranch_scc1 .LBB0_1203
	s_lshr_b32 s2, s2, 11
	s_mulk_i32 s2, 0x1800
	s_and_b64 s[0:1], s[0:1], exec
	s_cselect_b32 s0, s2, 0x18000
	s_ashr_i32 s1, s0, 31
	s_lshl_b64 s[0:1], s[0:1], 2
	s_add_u32 s2, s46, s0
	s_addc_u32 s3, s47, s1
	s_add_u32 s0, s2, 0x4000
	s_addc_u32 s1, s3, 0
	s_add_u32 s2, s2, 0x3000
	s_addc_u32 s3, s3, 0
	global_load_dwordx4 v[106:109], v[90:91], off
	global_load_dwordx4 v[110:113], v[90:91], off offset:16
	global_load_dwordx4 v[114:117], v[90:91], off offset:128
	global_load_dwordx4 v[118:121], v[90:91], off offset:144
	global_load_dwordx4 v[122:125], v[90:91], off offset:256
	global_load_dwordx4 v[126:129], v[90:91], off offset:272
	global_load_dwordx4 v[130:133], v[90:91], off offset:384
	global_load_dwordx4 v[134:137], v[90:91], off offset:400
	v_lshl_add_u64 v[50:51], s[0:1], 0, v[98:99]
	v_lshl_add_u64 v[58:59], s[0:1], 0, v[100:101]
	v_lshl_add_u64 v[62:63], v[92:93], 2, s[0:1]
	v_lshl_add_u64 v[66:67], s[0:1], 0, v[102:103]
	v_lshl_add_u64 v[70:71], v[94:95], 2, s[0:1]
	v_lshl_add_u64 v[74:75], s[0:1], 0, v[104:105]
	v_lshl_add_u64 v[78:79], v[96:97], 2, s[0:1]
	global_load_dwordx4 v[54:57], v[50:51], off offset:16
	s_nop 0
	global_load_dwordx4 v[50:53], v[50:51], off
	global_load_dwordx4 v[58:61], v[58:59], off
	global_load_dwordx4 v[62:65], v[62:63], off
	global_load_dwordx4 v[66:69], v[66:67], off
	global_load_dwordx4 v[70:73], v[70:71], off
	global_load_dwordx4 v[74:77], v[74:75], off
	global_load_dwordx4 v[78:81], v[78:79], off
	v_lshl_add_u64 v[22:23], s[2:3], 0, v[98:99]
	global_load_dwordx4 v[18:21], v[22:23], off offset:16
	s_nop 0
	global_load_dwordx4 v[22:25], v[22:23], off
	v_lshl_add_u64 v[30:31], s[2:3], 0, v[100:101]
	global_load_dwordx4 v[26:29], v[30:31], off offset:16
	s_nop 0
	global_load_dwordx4 v[30:33], v[30:31], off
	v_lshl_add_u64 v[38:39], s[2:3], 0, v[102:103]
	global_load_dwordx4 v[34:37], v[38:39], off offset:16
	s_nop 0
	global_load_dwordx4 v[38:41], v[38:39], off
	v_lshl_add_u64 v[46:47], s[2:3], 0, v[104:105]
	global_load_dwordx4 v[42:45], v[46:47], off offset:16
	s_nop 0
	global_load_dwordx4 v[46:49], v[46:47], off
	v_add_u32_e32 v138, s8, v158
	v_add_u32_e32 v140, s8, v82
	s_waitcnt vmcnt(0)
	v_pk_add_f32 v[50:51], v[50:51], 1.0 op_sel_hi:[1,0]
	v_pk_add_f32 v[52:53], v[52:53], 1.0 op_sel_hi:[1,0]
	v_pk_add_f32 v[54:55], v[54:55], 1.0 op_sel_hi:[1,0]
	v_pk_add_f32 v[56:57], v[56:57], 1.0 op_sel_hi:[1,0]
	v_pk_add_f32 v[58:59], v[58:59], 1.0 op_sel_hi:[1,0]
	v_pk_add_f32 v[60:61], v[60:61], 1.0 op_sel_hi:[1,0]
	v_pk_add_f32 v[62:63], v[62:63], 1.0 op_sel_hi:[1,0]
	v_pk_add_f32 v[64:65], v[64:65], 1.0 op_sel_hi:[1,0]
	v_pk_add_f32 v[66:67], v[66:67], 1.0 op_sel_hi:[1,0]
	v_pk_add_f32 v[68:69], v[68:69], 1.0 op_sel_hi:[1,0]
	v_pk_add_f32 v[70:71], v[70:71], 1.0 op_sel_hi:[1,0]
	v_pk_add_f32 v[72:73], v[72:73], 1.0 op_sel_hi:[1,0]
	v_pk_add_f32 v[74:75], v[74:75], 1.0 op_sel_hi:[1,0]
	v_pk_add_f32 v[76:77], v[76:77], 1.0 op_sel_hi:[1,0]
	v_pk_add_f32 v[78:79], v[78:79], 1.0 op_sel_hi:[1,0]
	v_pk_add_f32 v[80:81], v[80:81], 1.0 op_sel_hi:[1,0]
	v_pk_mul_f32 v[50:51], v[106:107], v[50:51]
	v_pk_mul_f32 v[106:107], v[108:109], v[52:53]
	v_pk_mul_f32 v[54:55], v[110:111], v[54:55]
	v_pk_mul_f32 v[110:111], v[112:113], v[56:57]
	v_pk_mul_f32 v[58:59], v[114:115], v[58:59]
	v_pk_mul_f32 v[114:115], v[116:117], v[60:61]
	v_pk_mul_f32 v[62:63], v[118:119], v[62:63]
	v_pk_mul_f32 v[118:119], v[120:121], v[64:65]
	v_pk_mul_f32 v[66:67], v[122:123], v[66:67]
	v_pk_mul_f32 v[122:123], v[124:125], v[68:69]
	v_pk_mul_f32 v[70:71], v[126:127], v[70:71]
	v_pk_mul_f32 v[126:127], v[128:129], v[72:73]
	v_pk_mul_f32 v[74:75], v[130:131], v[74:75]
	v_pk_mul_f32 v[130:131], v[132:133], v[76:77]
	v_pk_mul_f32 v[78:79], v[134:135], v[78:79]
	v_pk_mul_f32 v[134:135], v[136:137], v[80:81]
	v_mov_b64_e32 v[108:109], v[50:51]
	v_mov_b64_e32 v[112:113], v[54:55]
	v_mov_b64_e32 v[116:117], v[58:59]
	v_mov_b64_e32 v[120:121], v[62:63]
	v_mov_b64_e32 v[124:125], v[66:67]
	v_mov_b64_e32 v[128:129], v[70:71]
	v_mov_b64_e32 v[132:133], v[74:75]
	v_mov_b64_e32 v[136:137], v[78:79]
	v_and_b32_e32 v51, 64, v211
	v_add_u32_e32 v51, 64, v51
	v_xor_b32_e32 v50, 16, v211
	v_cmp_lt_i32_e32 vcc, v50, v51
	s_nop 1
	v_cndmask_b32_e32 v50, v211, v50, vcc
	v_lshlrev_b32_e32 v159, 2, v50
	v_xor_b32_e32 v50, 32, v211
	v_cmp_lt_i32_e32 vcc, v50, v51
	s_nop 1
	v_cndmask_b32_e32 v50, v211, v50, vcc
	v_lshlrev_b32_e32 v160, 2, v50
	v_xor_b32_e32 v50, 1, v211
	v_cmp_lt_i32_e32 vcc, v50, v51
	s_nop 1
	v_cndmask_b32_e32 v50, v211, v50, vcc
	v_lshlrev_b32_e32 v161, 2, v50
	v_xor_b32_e32 v50, 2, v211
	v_cmp_lt_i32_e32 vcc, v50, v51
	s_nop 1
	v_cndmask_b32_e32 v50, v211, v50, vcc
	v_lshlrev_b32_e32 v162, 2, v50
	v_xor_b32_e32 v50, 4, v211
	v_cmp_lt_i32_e32 vcc, v50, v51
	s_nop 1
	v_cndmask_b32_e32 v50, v211, v50, vcc
	v_lshlrev_b32_e32 v163, 2, v50
	v_xor_b32_e32 v50, 8, v211
	v_cmp_lt_i32_e32 vcc, v50, v51
	s_nop 1
	v_cndmask_b32_e32 v50, v211, v50, vcc
	v_lshlrev_b32_e32 v164, 2, v50
	v_mov_b64_e32 v[64:65], v[4:5]
	v_mov_b64_e32 v[60:61], v[8:9]
	v_mov_b64_e32 v[62:63], v[2:3]
	v_mov_b64_e32 v[58:59], v[6:7]
	v_mov_b64_e32 v[56:57], v[12:13]
	v_mov_b64_e32 v[54:55], v[10:11]
	v_mov_b64_e32 v[52:53], v[16:17]
	v_mov_b64_e32 v[50:51], v[14:15]
	s_add_i32 s2, s7, 1
	s_cmp_ge_i32 s2, s5
	v_add_u32_e32 v165, 16, v140
	s_cbranch_scc1 .LBB0_1208
	s_branch .LBB0_1207
